# GEMM2 K-loop: loop-invariant A-fragment LDS read addresses kept in spare VGPRs (same as GEMM1)
# baseline (speedup 1.0000x reference)
.LBB0_995:
	v_lshlrev_b32_e32 v4, 5, v0
	v_lshlrev_b32_e32 v2, 1, v0
	v_and_b32_e32 v4, 0xfffffc00, v4
	v_and_b32_e32 v3, 32, v2
	v_lshl_add_u32 v5, s2, 13, v4
	v_lshlrev_b32_e32 v0, 6, v0
	s_bfe_u32 s5, s61, 0x20006
	v_or_b32_e32 v6, v5, v3
	v_and_b32_e32 v0, 0x3c0, v0
	v_and_b32_e32 v2, 16, v2
	v_or3_b32 v6, v6, v0, v2
	v_lshl_add_u32 v4, s5, 12, v4
	v_or_b32_e32 v0, v0, v3
	v_or3_b32 v142, v0, v4, v2
	v_or_b32_e32 v0, 16, v0
	v_mov_b32_e32 v129, 0
	v_bitop3_b32 v5, v0, v5, v2 bitop3:0xde
	v_bitop3_b32 v143, v0, v4, v2 bitop3:0xde
	v_mbcnt_lo_u32_b32 v0, -1, 0
	v_mbcnt_hi_u32_b32 v0, -1, v0
	v_and_b32_e32 v4, 15, v0
	v_lshrrev_b32_e32 v0, 4, v0
	v_lshlrev_b32_e32 v0, 1, v0
	v_bfe_u32 v2, v4, 1, 3
	v_and_b32_e32 v2, 5, v2
	v_xor_b32_e32 v0, v0, v2
	v_lshlrev_b32_e32 v0, 4, v0
	v_lshl_add_u32 v0, v4, 7, v0
	v_lshl_add_u32 v6, s2, 13, v0
	v_xor_b32_e32 v5, 16, v6
	v_lshl_add_u32 v142, s5, 12, v0
	v_xor_b32_e32 v143, 16, v142
	s_waitcnt vmcnt(2)
	s_barrier
	s_mov_b64 s[14:15], 0x80
	v_lshl_add_u64 v[2:3], s[38:39], 0, v[128:129]
	s_add_i32 m0, s1, 0x18000
	v_lshl_add_u64 v[2:3], v[2:3], 0, s[14:15]
	s_lshl_b32 s52, s2, 6
	global_load_lds_dwordx4 v[2:3], off
	v_mov_b32_e32 v131, v129
	s_add_i32 m0, s1, 0x1a000
	s_add_u32 s2, s6, 0x5e000080
	v_lshl_add_u64 v[2:3], s[38:39], 0, v[130:131]
	v_lshl_add_u64 v[2:3], v[2:3], 0, s[14:15]
	s_addc_u32 s3, s7, 0
	s_add_i32 s53, s1, 0x8000
	global_load_lds_dwordx4 v[2:3], off
	s_mov_b32 m0, s53
	s_add_i32 s54, s1, 0xa000
	s_mov_b64 s[16:17], 0x5e000080
	global_load_lds_dwordx4 v132, s[2:3]
	s_mov_b32 m0, s54
	v_mov_b32_e32 v164, 0x24854
	global_load_lds_dwordx4 v134, s[2:3]
	s_add_u32 s2, s38, 0x4080
	s_addc_u32 s3, s39, 0
	s_add_i32 m0, s1, 0x1c000
	v_mov_b32_e32 v165, 0x24858
	global_load_lds_dwordx4 v128, s[2:3]
	s_add_i32 m0, s1, 0x1e000
	s_cmp_gt_u32 s61, 63
	global_load_lds_dwordx4 v130, s[2:3]
	v_readlane_b32 s2, v254, 10
	s_waitcnt vmcnt(6)
	s_cselect_b64 s[18:19], -1, 0
	s_cmp_eq_u32 s2, 1
	s_mov_b32 s2, 0x1a00000
	s_cselect_b32 s55, s2, 0x12000000
	s_cmpk_lt_u32 s61, 0x100
	v_mov_b32_e32 v136, v128
	s_cselect_b64 s[20:21], -1, 0
	s_lshl_b32 s56, s5, 6
	v_mov_b32_e32 v166, 0x2485c
	v_mov_b32_e32 v167, 0x24860
	v_mov_b32_e32 v168, 0x24864
	v_mov_b32_e32 v169, 0x24868
	v_mov_b32_e32 v170, 0x2486c
	v_mov_b32_e32 v171, 0x24870
	v_mov_b32_e32 v172, 0x24874
	v_mov_b32_e32 v173, 0x24878
	v_mov_b32_e32 v174, 0x2487c
	s_mov_b32 s57, 0x25800
	s_add_i32 s58, 0, 0x10000
	s_add_i32 s59, 0, 0x14000
	v_add_u32_e32 v164, 0x10000, v142
	v_add_u32_e32 v165, 0x10000, v143
	v_add_u32_e32 v166, 0x14000, v142
	v_add_u32_e32 v167, 0x14000, v143
	v_add_u32_e32 v168, 0x18000, v142
	v_add_u32_e32 v169, 0x18000, v143
	v_add_u32_e32 v170, 0x1c000, v142
	v_add_u32_e32 v171, 0x1c000, v143
	v_add_u32_e32 v175, 0, v6
	v_add_u32_e32 v176, 0, v5
	v_mov_b32_e32 v177, 0x7f7f7f7f
	s_mov_b64 s[22:23], 0x80000000
	s_mov_b32 s24, 0x3b800000
	v_mov_b32_e32 v128, v1
	v_mov_b32_e32 v0, v129
	v_mov_b32_e32 v1, v129
	v_mov_b32_e32 v2, v129
	v_mov_b32_e32 v3, v129
	v_mov_b32_e32 v4, v129
	v_mov_b32_e32 v5, v129
	v_mov_b32_e32 v6, v129
	v_mov_b32_e32 v7, v129
	v_mov_b32_e32 v8, v129
	v_mov_b32_e32 v9, v129
	v_mov_b32_e32 v10, v129
	v_mov_b32_e32 v11, v129
	v_mov_b32_e32 v12, v129
	v_mov_b32_e32 v13, v129
	v_mov_b32_e32 v14, v129
	v_mov_b32_e32 v15, v129
	v_mov_b32_e32 v16, v129
	v_mov_b32_e32 v17, v129
	v_mov_b32_e32 v18, v129
	v_mov_b32_e32 v19, v129
	v_mov_b32_e32 v20, v129
	v_mov_b32_e32 v21, v129
	v_mov_b32_e32 v22, v129
	v_mov_b32_e32 v23, v129
	v_mov_b32_e32 v24, v129
	v_mov_b32_e32 v25, v129
	v_mov_b32_e32 v26, v129
	v_mov_b32_e32 v27, v129
	v_mov_b32_e32 v28, v129
	v_mov_b32_e32 v29, v129
	v_mov_b32_e32 v30, v129
	v_mov_b32_e32 v31, v129
	v_mov_b32_e32 v36, v129
	v_mov_b32_e32 v37, v129
	v_mov_b32_e32 v38, v129
	v_mov_b32_e32 v39, v129
	v_mov_b32_e32 v44, v129
	v_mov_b32_e32 v45, v129
	v_mov_b32_e32 v46, v129
	v_mov_b32_e32 v47, v129
	v_mov_b32_e32 v32, v129
	v_mov_b32_e32 v33, v129
	v_mov_b32_e32 v34, v129
	v_mov_b32_e32 v35, v129
	v_mov_b32_e32 v40, v129
	v_mov_b32_e32 v41, v129
	v_mov_b32_e32 v42, v129
	v_mov_b32_e32 v43, v129
	v_mov_b32_e32 v48, v129
	v_mov_b32_e32 v49, v129
	v_mov_b32_e32 v50, v129
	v_mov_b32_e32 v51, v129
	v_mov_b32_e32 v52, v129
	v_mov_b32_e32 v53, v129
	v_mov_b32_e32 v54, v129
	v_mov_b32_e32 v55, v129
	v_mov_b32_e32 v56, v129
	v_mov_b32_e32 v57, v129
	v_mov_b32_e32 v58, v129
	v_mov_b32_e32 v59, v129
	v_mov_b32_e32 v60, v129
	v_mov_b32_e32 v61, v129
	v_mov_b32_e32 v62, v129
	v_mov_b32_e32 v63, v129
	v_mov_b32_e32 v64, v129
	v_mov_b32_e32 v65, v129
	v_mov_b32_e32 v66, v129
	v_mov_b32_e32 v67, v129
	v_mov_b32_e32 v68, v129
	v_mov_b32_e32 v69, v129
	v_mov_b32_e32 v70, v129
	v_mov_b32_e32 v71, v129
	v_mov_b32_e32 v72, v129
	v_mov_b32_e32 v73, v129
	v_mov_b32_e32 v74, v129
	v_mov_b32_e32 v75, v129
	v_mov_b32_e32 v76, v129
	v_mov_b32_e32 v77, v129
	v_mov_b32_e32 v78, v129
	v_mov_b32_e32 v79, v129
	v_mov_b32_e32 v80, v129
	v_mov_b32_e32 v81, v129
	v_mov_b32_e32 v82, v129
	v_mov_b32_e32 v83, v129
	v_mov_b32_e32 v84, v129
	v_mov_b32_e32 v85, v129
	v_mov_b32_e32 v86, v129
	v_mov_b32_e32 v87, v129
	v_mov_b32_e32 v88, v129
	v_mov_b32_e32 v89, v129
	v_mov_b32_e32 v90, v129
	v_mov_b32_e32 v91, v129
	v_mov_b32_e32 v92, v129
	v_mov_b32_e32 v93, v129
	v_mov_b32_e32 v94, v129
	v_mov_b32_e32 v95, v129
	v_mov_b32_e32 v96, v129
	v_mov_b32_e32 v97, v129
	v_mov_b32_e32 v98, v129
	v_mov_b32_e32 v99, v129
	v_mov_b32_e32 v100, v129
	v_mov_b32_e32 v101, v129
	v_mov_b32_e32 v102, v129
	v_mov_b32_e32 v103, v129
	v_mov_b32_e32 v104, v129
	v_mov_b32_e32 v105, v129
	v_mov_b32_e32 v106, v129
	v_mov_b32_e32 v107, v129
	v_mov_b32_e32 v108, v129
	v_mov_b32_e32 v109, v129
	v_mov_b32_e32 v110, v129
	v_mov_b32_e32 v111, v129
	v_mov_b32_e32 v112, v129
	v_mov_b32_e32 v113, v129
	v_mov_b32_e32 v114, v129
	v_mov_b32_e32 v115, v129
	v_mov_b32_e32 v116, v129
	v_mov_b32_e32 v117, v129
	v_mov_b32_e32 v118, v129
	v_mov_b32_e32 v119, v129
	v_mov_b32_e32 v120, v129
	v_mov_b32_e32 v121, v129
	v_mov_b32_e32 v122, v129
	v_mov_b32_e32 v123, v129
	v_mov_b32_e32 v124, v129
	v_mov_b32_e32 v125, v129
	v_mov_b32_e32 v126, v129
	v_mov_b32_e32 v127, v129
	s_barrier
	s_branch .LBB0_997

.LBB0_1008:
	s_add_u32 s5, s38, 0x100
	s_addc_u32 s27, s39, 0
	s_lshl_b32 s44, s61, 8
	s_lshl_b32 s29, s61, 19
	s_bitset1_b32 s44, 7
	s_mov_b32 s45, -2
	s_mov_b64 s[38:39], 0
	s_cmp_eq_u32 s45, 12
	s_cselect_b64 s[42:43], -1, 0
	s_and_b64 s[40:41], s[36:37], s[42:43]
	s_andn2_b64 vcc, exec, s[40:41]
	v_mov_b32_e32 v131, v138
	v_mov_b32_e32 v133, v128
	s_add_u32 s64, s6, s38
	ds_read_b128 v[178:181], v164
	ds_read_b128 v[186:189], v164 offset:2048
	ds_read_b128 v[182:185], v165
	ds_read_b128 v[190:193], v165 offset:2048
	s_addc_u32 s65, s7, s39
	ds_read_b128 v[194:197], v166
	ds_read_b128 v[202:205], v166 offset:2048
	ds_read_b128 v[198:201], v167
	ds_read_b128 v[206:209], v167 offset:2048
	s_add_u32 s66, s64, 0x5e000100
	s_addc_u32 s67, s65, 0
	s_and_b64 s[40:41], s[42:43], exec
	s_cselect_b32 s41, s11, s67
	s_cselect_b32 s40, s10, s66
	s_add_u32 s66, s5, s38
	s_addc_u32 s67, s27, s39
	s_and_b64 s[42:43], s[42:43], exec
	s_cselect_b32 s43, s35, s67
	s_cselect_b32 s42, s34, s66
	ds_read_b128 v[210:213], v175
	ds_read_b128 v[218:221], v175 offset:2048
	ds_read_b128 v[214:217], v176
	ds_read_b128 v[222:225], v176 offset:2048
	ds_read_b128 v[226:229], v175 offset:4096
	ds_read_b128 v[234:237], v175 offset:6144
	ds_read_b128 v[230:233], v176 offset:4096
	ds_read_b128 v[238:241], v176 offset:6144
	s_add_i32 m0, s1, 0xc000
	s_add_u32 vcc_lo, s64, s16
	s_addc_u32 vcc_hi, s65, s17
	global_load_lds_dwordx4 v128, vcc
	v_mov_b32_e32 v139, v129
	s_add_i32 m0, s1, 0xe000
	s_nop 0
	global_load_lds_dwordx4 v138, vcc
	s_waitcnt vmcnt(8)
	s_waitcnt lgkmcnt(0)
	s_barrier
	s_setprio 1
	s_waitcnt lgkmcnt(0)
	v_mfma_f32_16x16x128_f8f6f4 v[100:103], v[178:185], v[210:217], 0
	v_mfma_f32_16x16x128_f8f6f4 v[96:99], v[186:193], v[210:217], 0
	v_mfma_f32_16x16x128_f8f6f4 v[92:95], v[178:185], v[218:225], 0
	v_mfma_f32_16x16x128_f8f6f4 v[88:91], v[186:193], v[218:225], 0
	v_mfma_f32_16x16x128_f8f6f4 v[84:87], v[178:185], v[226:233], 0
	v_mfma_f32_16x16x128_f8f6f4 v[80:83], v[186:193], v[226:233], 0
	v_mfma_f32_16x16x128_f8f6f4 v[242:245], v[178:185], v[234:241], 0
	v_mfma_f32_16x16x128_f8f6f4 v[246:249], v[186:193], v[234:241], 0
	s_setprio 0
	s_setprio 1
	v_mfma_f32_16x16x128_f8f6f4 v[40:43], v[194:201], v[234:241], 0
	v_mfma_f32_16x16x128_f8f6f4 v[32:35], v[202:209], v[234:241], 0
	v_mfma_f32_16x16x128_f8f6f4 v[250:253], v[194:201], v[210:217], 0
	v_mfma_f32_16x16x128_f8f6f4 v[144:147], v[202:209], v[210:217], 0
	v_mfma_f32_16x16x128_f8f6f4 v[148:151], v[194:201], v[218:225], 0
	v_mfma_f32_16x16x128_f8f6f4 v[152:155], v[202:209], v[218:225], 0
	v_mfma_f32_16x16x128_f8f6f4 v[156:159], v[194:201], v[226:233], 0
	v_mfma_f32_16x16x128_f8f6f4 v[160:163], v[202:209], v[226:233], 0
	s_setprio 0
	s_barrier
	s_add_i32 s64, s58, s48
	s_mov_b32 m0, s64
	s_nop 2
	ds_read_b128 v[48:51], v175 offset:16384
	ds_read_b128 v[56:59], v175 offset:18432
	ds_read_b128 v[52:55], v176 offset:16384
	ds_read_b128 v[60:63], v176 offset:18432
	ds_read_b128 v[64:67], v175 offset:20480
	ds_read_b128 v[72:75], v175 offset:22528
	ds_read_b128 v[68:71], v176 offset:20480
	ds_read_b128 v[76:79], v176 offset:22528
	s_nop 0
	global_load_lds_dwordx4 v136, s[42:43]
	s_add_i32 m0, s64, 0x2000
	s_add_u32 s64, s42, 0x4000
	s_addc_u32 s65, s43, 0
	s_add_i32 s66, s59, s48
	s_nop 0
	global_load_lds_dwordx4 v130, s[42:43]
	s_mov_b32 m0, s66
	s_nop 0
	global_load_lds_dwordx4 v136, s[64:65]
	s_add_i32 m0, s66, 0x2000
	s_nop 0
	global_load_lds_dwordx4 v130, s[64:65]
	s_waitcnt vmcnt(6)
	s_waitcnt lgkmcnt(0)
	s_barrier
	s_setprio 1
	s_waitcnt lgkmcnt(0)
	v_mfma_f32_16x16x128_f8f6f4 v[44:47], v[178:185], v[48:55], 0
	v_mfma_f32_16x16x128_f8f6f4 v[36:39], v[186:193], v[48:55], 0
	v_mfma_f32_16x16x128_f8f6f4 v[28:31], v[178:185], v[56:63], 0
	v_mfma_f32_16x16x128_f8f6f4 v[24:27], v[186:193], v[56:63], 0
	v_mfma_f32_16x16x128_f8f6f4 v[20:23], v[178:185], v[64:71], 0
	v_mfma_f32_16x16x128_f8f6f4 v[16:19], v[186:193], v[64:71], 0
	v_mfma_f32_16x16x128_f8f6f4 v[12:15], v[178:185], v[72:79], 0
	v_mfma_f32_16x16x128_f8f6f4 v[8:11], v[186:193], v[72:79], 0
	s_setprio 0
	s_setprio 1
	v_mfma_f32_16x16x128_f8f6f4 v[4:7], v[194:201], v[48:55], 0
	v_mfma_f32_16x16x128_f8f6f4 v[0:3], v[202:209], v[48:55], 0
	v_mfma_f32_16x16x128_f8f6f4 v[104:107], v[194:201], v[56:63], 0
	v_mfma_f32_16x16x128_f8f6f4 v[108:111], v[202:209], v[56:63], 0
	v_mfma_f32_16x16x128_f8f6f4 v[112:115], v[194:201], v[64:71], 0
	v_mfma_f32_16x16x128_f8f6f4 v[116:119], v[202:209], v[64:71], 0
	v_mfma_f32_16x16x128_f8f6f4 v[120:123], v[194:201], v[72:79], 0
	v_mfma_f32_16x16x128_f8f6f4 v[124:127], v[202:209], v[72:79], 0
	s_setprio 0
	s_barrier
	s_add_i32 s64, 0, 0x18000
	s_add_i32 s65, 0, 0x1c000
	ds_read_b128 v[178:181], v168
	ds_read_b128 v[186:189], v168 offset:2048
	ds_read_b128 v[182:185], v169
	ds_read_b128 v[190:193], v169 offset:2048
	ds_read_b128 v[194:197], v170
	ds_read_b128 v[202:205], v170 offset:2048
	ds_read_b128 v[198:201], v171
	ds_read_b128 v[206:209], v171 offset:2048
	s_mov_b32 m0, s50
	v_mov_b32_e32 v128, v133
	ds_read_b128 v[48:51], v175 offset:32768
	ds_read_b128 v[210:213], v175 offset:34816
	ds_read_b128 v[52:55], v176 offset:32768
	ds_read_b128 v[214:217], v176 offset:34816
	ds_read_b128 v[218:221], v175 offset:36864
	ds_read_b128 v[226:229], v175 offset:38912
	ds_read_b128 v[222:225], v176 offset:36864
	ds_read_b128 v[230:233], v176 offset:38912
	s_mov_b32 m0, s1
	s_nop 0
	global_load_lds_dwordx4 v132, s[40:41]
	s_mov_b32 m0, s49
	s_nop 0
	global_load_lds_dwordx4 v134, s[40:41]
	s_mov_b32 m0, s50
	v_mov_b32_e32 v138, v131
	global_load_lds_dwordx4 v128, s[40:41]
	s_mov_b32 m0, s51
	s_nop 0
	global_load_lds_dwordx4 v138, s[40:41]
	s_waitcnt vmcnt(8)
	s_waitcnt lgkmcnt(0)
	s_barrier
	s_setprio 1
	s_waitcnt lgkmcnt(0)
	v_mfma_f32_16x16x128_f8f6f4 v[100:103], v[178:185], v[48:55], v[100:103]
	v_mfma_f32_16x16x128_f8f6f4 v[96:99], v[186:193], v[48:55], v[96:99]
	v_mfma_f32_16x16x128_f8f6f4 v[92:95], v[178:185], v[210:217], v[92:95]
	v_mfma_f32_16x16x128_f8f6f4 v[88:91], v[186:193], v[210:217], v[88:91]
	v_mfma_f32_16x16x128_f8f6f4 v[84:87], v[178:185], v[218:225], v[84:87]
	v_mfma_f32_16x16x128_f8f6f4 v[80:83], v[186:193], v[218:225], v[80:83]
	v_mfma_f32_16x16x128_f8f6f4 v[76:79], v[178:185], v[226:233], v[242:245]
	v_mfma_f32_16x16x128_f8f6f4 v[72:75], v[186:193], v[226:233], v[246:249]
	s_setprio 0
	s_setprio 1
	v_mfma_f32_16x16x128_f8f6f4 v[68:71], v[194:201], v[48:55], v[250:253]
	v_mfma_f32_16x16x128_f8f6f4 v[64:67], v[202:209], v[48:55], v[144:147]
	v_mfma_f32_16x16x128_f8f6f4 v[60:63], v[194:201], v[210:217], v[148:151]
	v_mfma_f32_16x16x128_f8f6f4 v[56:59], v[202:209], v[210:217], v[152:155]
	v_mfma_f32_16x16x128_f8f6f4 v[52:55], v[194:201], v[218:225], v[156:159]
	v_mfma_f32_16x16x128_f8f6f4 v[48:51], v[202:209], v[218:225], v[160:163]
	v_mfma_f32_16x16x128_f8f6f4 v[40:43], v[194:201], v[226:233], v[40:43]
	v_mfma_f32_16x16x128_f8f6f4 v[32:35], v[202:209], v[226:233], v[32:35]
	s_setprio 0
	s_barrier
	v_mov_b32_e32 v137, v129
	ds_read_b128 v[210:213], v175 offset:49152
	ds_read_b128 v[218:221], v175 offset:51200
	ds_read_b128 v[214:217], v176 offset:49152
	ds_read_b128 v[222:225], v176 offset:51200
	ds_read_b128 v[226:229], v175 offset:53248
	ds_read_b128 v[234:237], v175 offset:55296
	ds_read_b128 v[230:233], v176 offset:53248
	ds_read_b128 v[238:241], v176 offset:55296
	s_add_i32 s64, s64, s48
	s_add_u32 vcc_lo, s42, s14
	s_addc_u32 vcc_hi, s43, s15
	s_mov_b32 m0, s64
	v_mov_b32_e32 v131, v129
	global_load_lds_dwordx4 v136, vcc
	s_add_i32 m0, s64, 0x2000
	v_mov_b32_e32 v133, v129
	s_add_u32 s42, s42, 0x4080
	s_addc_u32 s43, s43, 0
	s_add_i32 s64, s65, s48
	global_load_lds_dwordx4 v130, vcc
	s_mov_b32 m0, s64
	v_mov_b32_e32 v135, v129
	global_load_lds_dwordx4 v136, s[42:43]
	s_add_i32 m0, s64, 0x2000
	s_nop 0
	global_load_lds_dwordx4 v130, s[42:43]
	s_mov_b32 m0, s53
	s_add_u32 vcc_lo, s40, s14
	s_addc_u32 vcc_hi, s41, s15
	global_load_lds_dwordx4 v132, vcc
	s_mov_b32 m0, s54
	s_nop 0
	global_load_lds_dwordx4 v134, vcc
	s_waitcnt vmcnt(8)
	s_waitcnt lgkmcnt(0)
	s_barrier
	s_setprio 1
	s_waitcnt lgkmcnt(0)
	v_mfma_f32_16x16x128_f8f6f4 v[44:47], v[178:185], v[210:217], v[44:47]
	v_mfma_f32_16x16x128_f8f6f4 v[36:39], v[186:193], v[210:217], v[36:39]
	v_mfma_f32_16x16x128_f8f6f4 v[28:31], v[178:185], v[218:225], v[28:31]
	v_mfma_f32_16x16x128_f8f6f4 v[24:27], v[186:193], v[218:225], v[24:27]
	v_mfma_f32_16x16x128_f8f6f4 v[20:23], v[178:185], v[226:233], v[20:23]
	v_mfma_f32_16x16x128_f8f6f4 v[16:19], v[186:193], v[226:233], v[16:19]
	v_mfma_f32_16x16x128_f8f6f4 v[12:15], v[178:185], v[234:241], v[12:15]
	v_mfma_f32_16x16x128_f8f6f4 v[8:11], v[186:193], v[234:241], v[8:11]
	s_setprio 0
	s_setprio 1
	v_mfma_f32_16x16x128_f8f6f4 v[4:7], v[194:201], v[210:217], v[4:7]
	v_mfma_f32_16x16x128_f8f6f4 v[0:3], v[202:209], v[210:217], v[0:3]
	v_mfma_f32_16x16x128_f8f6f4 v[104:107], v[194:201], v[218:225], v[104:107]
	v_mfma_f32_16x16x128_f8f6f4 v[108:111], v[202:209], v[218:225], v[108:111]
	v_mfma_f32_16x16x128_f8f6f4 v[112:115], v[194:201], v[226:233], v[112:115]
	v_mfma_f32_16x16x128_f8f6f4 v[116:119], v[202:209], v[226:233], v[116:119]
	v_mfma_f32_16x16x128_f8f6f4 v[120:123], v[194:201], v[234:241], v[120:123]
	v_mfma_f32_16x16x128_f8f6f4 v[124:127], v[202:209], v[234:241], v[124:127]
	s_setprio 0
	s_barrier
	s_add_i32 s45, s45, 2
	s_add_u32 s38, s38, 0x100
	s_addc_u32 s39, s39, 0
	s_branch .LBB0_1010
.LBB0_1009:
	s_add_u32 s64, s6, s38
	ds_read_b128 v[178:181], v164
	ds_read_b128 v[186:189], v164 offset:2048
	ds_read_b128 v[182:185], v165
	ds_read_b128 v[190:193], v165 offset:2048
	s_addc_u32 s65, s7, s39
	ds_read_b128 v[194:197], v166
	ds_read_b128 v[202:205], v166 offset:2048
	ds_read_b128 v[198:201], v167
	ds_read_b128 v[206:209], v167 offset:2048
	s_add_u32 s66, s64, 0x5e000100
	s_addc_u32 s67, s65, 0
	s_and_b64 s[40:41], s[42:43], exec
	s_cselect_b32 s41, s11, s67
	s_cselect_b32 s40, s10, s66
	s_add_u32 s66, s5, s38
	s_addc_u32 s67, s27, s39
	s_and_b64 s[42:43], s[42:43], exec
	s_cselect_b32 s43, s35, s67
	s_cselect_b32 s42, s34, s66
	ds_read_b128 v[210:213], v175
	ds_read_b128 v[218:221], v175 offset:2048
	ds_read_b128 v[214:217], v176
	ds_read_b128 v[222:225], v176 offset:2048
	ds_read_b128 v[226:229], v175 offset:4096
	ds_read_b128 v[234:237], v175 offset:6144
	ds_read_b128 v[230:233], v176 offset:4096
	ds_read_b128 v[238:241], v176 offset:6144
	s_add_i32 m0, s1, 0xc000
	s_add_u32 vcc_lo, s64, s16
	s_addc_u32 vcc_hi, s65, s17
	global_load_lds_dwordx4 v128, vcc
	v_mov_b32_e32 v139, v129
	s_add_i32 m0, s1, 0xe000
	s_nop 0
	global_load_lds_dwordx4 v138, vcc
	s_waitcnt vmcnt(8)
	s_waitcnt lgkmcnt(0)
	s_barrier
	s_setprio 1
	s_waitcnt lgkmcnt(0)
	v_mfma_f32_16x16x128_f8f6f4 v[100:103], v[178:185], v[210:217], v[100:103]
	v_mfma_f32_16x16x128_f8f6f4 v[96:99], v[186:193], v[210:217], v[96:99]
	v_mfma_f32_16x16x128_f8f6f4 v[92:95], v[178:185], v[218:225], v[92:95]
	v_mfma_f32_16x16x128_f8f6f4 v[88:91], v[186:193], v[218:225], v[88:91]
	v_mfma_f32_16x16x128_f8f6f4 v[84:87], v[178:185], v[226:233], v[84:87]
	v_mfma_f32_16x16x128_f8f6f4 v[80:83], v[186:193], v[226:233], v[80:83]
	v_mfma_f32_16x16x128_f8f6f4 v[242:245], v[178:185], v[234:241], v[76:79]
	v_mfma_f32_16x16x128_f8f6f4 v[246:249], v[186:193], v[234:241], v[72:75]
	s_setprio 0
	s_setprio 1
	v_mfma_f32_16x16x128_f8f6f4 v[40:43], v[194:201], v[234:241], v[40:43]
	v_mfma_f32_16x16x128_f8f6f4 v[32:35], v[202:209], v[234:241], v[32:35]
	v_mfma_f32_16x16x128_f8f6f4 v[250:253], v[194:201], v[210:217], v[68:71]
	v_mfma_f32_16x16x128_f8f6f4 v[144:147], v[202:209], v[210:217], v[64:67]
	v_mfma_f32_16x16x128_f8f6f4 v[148:151], v[194:201], v[218:225], v[60:63]
	v_mfma_f32_16x16x128_f8f6f4 v[152:155], v[202:209], v[218:225], v[56:59]
	v_mfma_f32_16x16x128_f8f6f4 v[156:159], v[194:201], v[226:233], v[52:55]
	v_mfma_f32_16x16x128_f8f6f4 v[160:163], v[202:209], v[226:233], v[48:51]
	s_setprio 0
	s_barrier
	s_add_i32 s64, s58, s48
	s_mov_b32 m0, s64
	s_nop 2
	ds_read_b128 v[48:51], v175 offset:16384
	ds_read_b128 v[56:59], v175 offset:18432
	ds_read_b128 v[52:55], v176 offset:16384
	ds_read_b128 v[60:63], v176 offset:18432
	ds_read_b128 v[64:67], v175 offset:20480
	ds_read_b128 v[72:75], v175 offset:22528
	ds_read_b128 v[68:71], v176 offset:20480
	ds_read_b128 v[76:79], v176 offset:22528
	s_nop 0
	global_load_lds_dwordx4 v136, s[42:43]
	s_add_i32 m0, s64, 0x2000
	s_add_u32 s64, s42, 0x4000
	s_addc_u32 s65, s43, 0
	s_add_i32 s66, s59, s48
	s_nop 0
	global_load_lds_dwordx4 v130, s[42:43]
	s_mov_b32 m0, s66
	s_nop 0
	global_load_lds_dwordx4 v136, s[64:65]
	s_add_i32 m0, s66, 0x2000
	s_nop 0
	global_load_lds_dwordx4 v130, s[64:65]
	s_waitcnt vmcnt(6)
	s_waitcnt lgkmcnt(0)
	s_barrier
	s_setprio 1
	s_waitcnt lgkmcnt(0)
	v_mfma_f32_16x16x128_f8f6f4 v[44:47], v[178:185], v[48:55], v[44:47]
	v_mfma_f32_16x16x128_f8f6f4 v[36:39], v[186:193], v[48:55], v[36:39]
	v_mfma_f32_16x16x128_f8f6f4 v[28:31], v[178:185], v[56:63], v[28:31]
	v_mfma_f32_16x16x128_f8f6f4 v[24:27], v[186:193], v[56:63], v[24:27]
	v_mfma_f32_16x16x128_f8f6f4 v[20:23], v[178:185], v[64:71], v[20:23]
	v_mfma_f32_16x16x128_f8f6f4 v[16:19], v[186:193], v[64:71], v[16:19]
	v_mfma_f32_16x16x128_f8f6f4 v[12:15], v[178:185], v[72:79], v[12:15]
	v_mfma_f32_16x16x128_f8f6f4 v[8:11], v[186:193], v[72:79], v[8:11]
	s_setprio 0
	s_setprio 1
	v_mfma_f32_16x16x128_f8f6f4 v[4:7], v[194:201], v[48:55], v[4:7]
	v_mfma_f32_16x16x128_f8f6f4 v[0:3], v[202:209], v[48:55], v[0:3]
	v_mfma_f32_16x16x128_f8f6f4 v[104:107], v[194:201], v[56:63], v[104:107]
	v_mfma_f32_16x16x128_f8f6f4 v[108:111], v[202:209], v[56:63], v[108:111]
	v_mfma_f32_16x16x128_f8f6f4 v[112:115], v[194:201], v[64:71], v[112:115]
	v_mfma_f32_16x16x128_f8f6f4 v[116:119], v[202:209], v[64:71], v[116:119]
	v_mfma_f32_16x16x128_f8f6f4 v[120:123], v[194:201], v[72:79], v[120:123]
	v_mfma_f32_16x16x128_f8f6f4 v[124:127], v[202:209], v[72:79], v[124:127]
	s_setprio 0
	s_barrier
	s_add_i32 s64, 0, 0x18000
	s_add_i32 s65, 0, 0x1c000
	ds_read_b128 v[178:181], v168
	ds_read_b128 v[186:189], v168 offset:2048
	ds_read_b128 v[182:185], v169
	ds_read_b128 v[190:193], v169 offset:2048
	ds_read_b128 v[194:197], v170
	ds_read_b128 v[202:205], v170 offset:2048
	ds_read_b128 v[198:201], v171
	ds_read_b128 v[206:209], v171 offset:2048
	s_mov_b32 m0, s50
	v_mov_b32_e32 v128, v133
	ds_read_b128 v[48:51], v175 offset:32768
	ds_read_b128 v[210:213], v175 offset:34816
	ds_read_b128 v[52:55], v176 offset:32768
	ds_read_b128 v[214:217], v176 offset:34816
	ds_read_b128 v[218:221], v175 offset:36864
	ds_read_b128 v[226:229], v175 offset:38912
	ds_read_b128 v[222:225], v176 offset:36864
	ds_read_b128 v[230:233], v176 offset:38912
	s_mov_b32 m0, s1
	s_nop 0
	global_load_lds_dwordx4 v132, s[40:41]
	s_mov_b32 m0, s49
	s_nop 0
	global_load_lds_dwordx4 v134, s[40:41]
	s_mov_b32 m0, s50
	v_mov_b32_e32 v138, v131
	global_load_lds_dwordx4 v128, s[40:41]
	s_mov_b32 m0, s51
	s_nop 0
	global_load_lds_dwordx4 v138, s[40:41]
	s_waitcnt vmcnt(8)
	s_waitcnt lgkmcnt(0)
	s_barrier
	s_setprio 1
	s_waitcnt lgkmcnt(0)
	v_mfma_f32_16x16x128_f8f6f4 v[100:103], v[178:185], v[48:55], v[100:103]
	v_mfma_f32_16x16x128_f8f6f4 v[96:99], v[186:193], v[48:55], v[96:99]
	v_mfma_f32_16x16x128_f8f6f4 v[92:95], v[178:185], v[210:217], v[92:95]
	v_mfma_f32_16x16x128_f8f6f4 v[88:91], v[186:193], v[210:217], v[88:91]
	v_mfma_f32_16x16x128_f8f6f4 v[84:87], v[178:185], v[218:225], v[84:87]
	v_mfma_f32_16x16x128_f8f6f4 v[80:83], v[186:193], v[218:225], v[80:83]
	v_mfma_f32_16x16x128_f8f6f4 v[76:79], v[178:185], v[226:233], v[242:245]
	v_mfma_f32_16x16x128_f8f6f4 v[72:75], v[186:193], v[226:233], v[246:249]
	s_setprio 0
	s_setprio 1
	v_mfma_f32_16x16x128_f8f6f4 v[68:71], v[194:201], v[48:55], v[250:253]
	v_mfma_f32_16x16x128_f8f6f4 v[64:67], v[202:209], v[48:55], v[144:147]
	v_mfma_f32_16x16x128_f8f6f4 v[60:63], v[194:201], v[210:217], v[148:151]
	v_mfma_f32_16x16x128_f8f6f4 v[56:59], v[202:209], v[210:217], v[152:155]
	v_mfma_f32_16x16x128_f8f6f4 v[52:55], v[194:201], v[218:225], v[156:159]
	v_mfma_f32_16x16x128_f8f6f4 v[48:51], v[202:209], v[218:225], v[160:163]
	v_mfma_f32_16x16x128_f8f6f4 v[40:43], v[194:201], v[226:233], v[40:43]
	v_mfma_f32_16x16x128_f8f6f4 v[32:35], v[202:209], v[226:233], v[32:35]
	s_setprio 0
	s_barrier
	v_mov_b32_e32 v137, v129
	ds_read_b128 v[210:213], v175 offset:49152
	ds_read_b128 v[218:221], v175 offset:51200
	ds_read_b128 v[214:217], v176 offset:49152
	ds_read_b128 v[222:225], v176 offset:51200
	ds_read_b128 v[226:229], v175 offset:53248
	ds_read_b128 v[234:237], v175 offset:55296
	ds_read_b128 v[230:233], v176 offset:53248
	ds_read_b128 v[238:241], v176 offset:55296
	s_add_i32 s64, s64, s48
	s_add_u32 vcc_lo, s42, s14
	s_addc_u32 vcc_hi, s43, s15
	s_mov_b32 m0, s64
	v_mov_b32_e32 v131, v129
	global_load_lds_dwordx4 v136, vcc
	s_add_i32 m0, s64, 0x2000
	v_mov_b32_e32 v133, v129
	s_add_u32 s42, s42, 0x4080
	s_addc_u32 s43, s43, 0
	s_add_i32 s64, s65, s48
	global_load_lds_dwordx4 v130, vcc
	s_mov_b32 m0, s64
	v_mov_b32_e32 v135, v129
	global_load_lds_dwordx4 v136, s[42:43]
	s_add_i32 m0, s64, 0x2000
	s_nop 0
	global_load_lds_dwordx4 v130, s[42:43]
	s_mov_b32 m0, s53
	s_add_u32 vcc_lo, s40, s14
	s_addc_u32 vcc_hi, s41, s15
	global_load_lds_dwordx4 v132, vcc
	s_mov_b32 m0, s54
	s_nop 0
	global_load_lds_dwordx4 v134, vcc
	s_waitcnt vmcnt(8)
	s_waitcnt lgkmcnt(0)
	s_barrier
	s_setprio 1
	s_waitcnt lgkmcnt(0)
	v_mfma_f32_16x16x128_f8f6f4 v[44:47], v[178:185], v[210:217], v[44:47]
	v_mfma_f32_16x16x128_f8f6f4 v[36:39], v[186:193], v[210:217], v[36:39]
	v_mfma_f32_16x16x128_f8f6f4 v[28:31], v[178:185], v[218:225], v[28:31]
	v_mfma_f32_16x16x128_f8f6f4 v[24:27], v[186:193], v[218:225], v[24:27]
	v_mfma_f32_16x16x128_f8f6f4 v[20:23], v[178:185], v[226:233], v[20:23]
	v_mfma_f32_16x16x128_f8f6f4 v[16:19], v[186:193], v[226:233], v[16:19]
	v_mfma_f32_16x16x128_f8f6f4 v[12:15], v[178:185], v[234:241], v[12:15]
	v_mfma_f32_16x16x128_f8f6f4 v[8:11], v[186:193], v[234:241], v[8:11]
	s_setprio 0
	s_setprio 1
	v_mfma_f32_16x16x128_f8f6f4 v[4:7], v[194:201], v[210:217], v[4:7]
	v_mfma_f32_16x16x128_f8f6f4 v[0:3], v[202:209], v[210:217], v[0:3]
	v_mfma_f32_16x16x128_f8f6f4 v[104:107], v[194:201], v[218:225], v[104:107]
	v_mfma_f32_16x16x128_f8f6f4 v[108:111], v[202:209], v[218:225], v[108:111]
	v_mfma_f32_16x16x128_f8f6f4 v[112:115], v[194:201], v[226:233], v[112:115]
	v_mfma_f32_16x16x128_f8f6f4 v[116:119], v[202:209], v[226:233], v[116:119]
	v_mfma_f32_16x16x128_f8f6f4 v[120:123], v[194:201], v[234:241], v[120:123]
	v_mfma_f32_16x16x128_f8f6f4 v[124:127], v[202:209], v[234:241], v[124:127]
	s_setprio 0
	s_barrier
	s_add_i32 s45, s45, 2
	s_add_u32 s38, s38, 0x100
	s_addc_u32 s39, s39, 0
	s_cmp_gt_u32 s45, 13
	s_cbranch_scc1 .LBB0_1012
